# v44 + grid barrier: every waiter polls the TOP arrival counter (>= (gen+1)*nx); last XCD leader no longer bumps the generation word
# speedup vs baseline: 1.0024x; 1.0024x over previous
; __device__ __forceinline__ unsigned xb_ld(unsigned* p)              { return __hip_atomic_load(p, __ATOMIC_RELAXED, __HIP_MEMORY_SCOPE_AGENT); }
; __device__ __forceinline__ unsigned xb_add(unsigned* p, unsigned v) { return __hip_atomic_fetch_add(p, v, __ATOMIC_RELAXED, __HIP_MEMORY_SCOPE_AGENT); }
; #define XB_SPIN(cond, bar) do { unsigned _sp = 0; while (cond) { __builtin_amdgcn_s_sleep(1); \
;     if ((++_sp & 255u) == 0u) { if (xb_ld(&(bar)[XB_TMO])) break; if (_sp > XB_SPIN_CAP) { atomicAdd(&(bar)[XB_TMO], 1u); break; } } } } while (0)
; __device__ __forceinline__ void xcd_barrier(const XcdBarrier& b) {
;     ...
;         const unsigned old = xb_add(&bar[XB_XSUB(b.x)], 1u);
;         const unsigned gen = old / nloc;
;         if (old + 1u == (gen + 1u) * nloc) {
;             __builtin_amdgcn_fence(__ATOMIC_RELEASE, "agent");
;             asm volatile("s_waitcnt vmcnt(0)" ::: "memory");
;             const unsigned og = xb_add(&bar[XB_TOP], 1u);
;             const unsigned tg = og / nx;
;             if (og + 1u == (tg + 1u) * nx) xb_add(&bar[XB_TOPGEN], 1u);
;             else XB_SPIN(xb_ld(&bar[XB_TOPGEN]) == tg, bar);
;             __builtin_amdgcn_fence(__ATOMIC_ACQUIRE, "agent");
;             xb_add(&bar[XB_XGEN(b.x)], 1u);
;             asm volatile("s_waitcnt vmcnt(0)" ::: "memory");
;         } else {
;             XB_SPIN(xb_ld(&bar[XB_XGEN(b.x)]) == gen, bar);
.LBB0_108:
	s_lshl_b32 s20, s33, 6
	s_add_i32 s2, s20, 0x500
	s_mov_b32 s3, 0
	s_lshl_b64 s[0:1], s[2:3], 2
	s_add_u32 s0, s30, s0
	s_addc_u32 s1, s31, s1
	v_mov_b32_e32 v1, 1
	v_mov_b64_e32 v[6:7], s[0:1]
	flat_atomic_add v1, v[6:7], v1 sc0
	v_cvt_f32_u32_e32 v3, v4
	v_sub_u32_e32 v5, 0, v4
	v_rcp_iflag_f32_e32 v3, v3
	s_nop 0
	v_mul_f32_e32 v3, 0x4f7ffffe, v3
	v_cvt_u32_f32_e32 v3, v3
	v_mul_lo_u32 v5, v5, v3
	v_mul_hi_u32 v5, v3, v5
	v_add_u32_e32 v3, v3, v5
	s_waitcnt vmcnt(0) lgkmcnt(0)
	v_mul_hi_u32 v3, v1, v3
	v_mul_lo_u32 v5, v3, v4
	v_add_u32_e32 v6, 1, v1
	v_sub_u32_e32 v1, v1, v5
	v_add_u32_e32 v7, 1, v3
	v_cmp_ge_u32_e32 vcc, v1, v4
	v_sub_u32_e32 v5, v1, v4
	s_nop 0
	v_cndmask_b32_e32 v3, v3, v7, vcc
	v_cndmask_b32_e32 v1, v1, v5, vcc
	v_add_u32_e32 v5, 1, v3
	v_cmp_ge_u32_e32 vcc, v1, v4
	s_nop 1
	v_cndmask_b32_e32 v1, v3, v5, vcc
	v_mad_u64_u32 v[4:5], s[0:1], v4, v1, v[4:5]
	v_cmp_ne_u32_e32 vcc, v6, v4
	s_and_saveexec_b64 s[0:1], vcc
	s_xor_b64 s[0:1], exec, s[0:1]
	s_cbranch_execz .LBB0_121
	v_mad_u32_u24 v1, v1, v2, v2
	s_movk_i32 s2, 0xd00
	s_lshl_b64 s[2:3], s[2:3], 2
	s_add_u32 s4, s30, s2
	s_addc_u32 s5, s31, s3
	v_mov_b64_e32 v[2:3], s[4:5]
	flat_load_dword v2, v[2:3] sc1
	s_waitcnt vmcnt(0) lgkmcnt(0)
	v_cmp_gt_u32_e32 vcc, v1, v2
	s_and_saveexec_b64 s[2:3], vcc
	s_cbranch_execz .LBB0_120
	s_mov_b32 s21, 1
	s_mov_b64 s[6:7], 0
	s_branch .LBB0_112

; __device__ __forceinline__ unsigned xb_ld(unsigned* p)              { return __hip_atomic_load(p, __ATOMIC_RELAXED, __HIP_MEMORY_SCOPE_AGENT); }
; #define XB_SPIN(cond, bar) do { unsigned _sp = 0; while (cond) { __builtin_amdgcn_s_sleep(1); \
;     if ((++_sp & 255u) == 0u) { if (xb_ld(&(bar)[XB_TMO])) break; if (_sp > XB_SPIN_CAP) { atomicAdd(&(bar)[XB_TMO], 1u); break; } } } } while (0)
; __device__ __forceinline__ void xcd_barrier(const XcdBarrier& b) {
;     ...
;             XB_SPIN(xb_ld(&bar[XB_XGEN(b.x)]) == gen, bar);
.LBB0_116:
	s_andn2_b64 s[10:11], s[10:11], exec
	s_and_b64 s[16:17], s[16:17], exec
	s_or_b64 s[10:11], s[10:11], s[16:17]
	s_and_saveexec_b64 s[16:17], s[14:15]
	s_cbranch_execz .LBB0_111
	v_mov_b64_e32 v[2:3], s[4:5]
	flat_load_dword v2, v[2:3] sc1
	s_add_i32 s21, s21, 1
	s_or_b64 s[10:11], s[10:11], exec
	s_waitcnt vmcnt(0) lgkmcnt(0)
	v_cmp_le_u32_e32 vcc, v1, v2
	s_orn2_b64 s[12:13], vcc, exec
	s_branch .LBB0_111

; __device__ __forceinline__ unsigned xb_ld(unsigned* p)              { return __hip_atomic_load(p, __ATOMIC_RELAXED, __HIP_MEMORY_SCOPE_AGENT); }
; __device__ __forceinline__ unsigned xb_add(unsigned* p, unsigned v) { return __hip_atomic_fetch_add(p, v, __ATOMIC_RELAXED, __HIP_MEMORY_SCOPE_AGENT); }
; #define XB_SPIN(cond, bar) do { unsigned _sp = 0; while (cond) { __builtin_amdgcn_s_sleep(1); \
;     if ((++_sp & 255u) == 0u) { if (xb_ld(&(bar)[XB_TMO])) break; if (_sp > XB_SPIN_CAP) { atomicAdd(&(bar)[XB_TMO], 1u); break; } } } } while (0)
; __device__ __forceinline__ void xcd_barrier(const XcdBarrier& b) {
;     ...
;         if (old + 1u == (gen + 1u) * nloc) {
;             __builtin_amdgcn_fence(__ATOMIC_RELEASE, "agent");
;             asm volatile("s_waitcnt vmcnt(0)" ::: "memory");
;             const unsigned og = xb_add(&bar[XB_TOP], 1u);
;             const unsigned tg = og / nx;
;             if (og + 1u == (tg + 1u) * nx) xb_add(&bar[XB_TOPGEN], 1u);
;             else XB_SPIN(xb_ld(&bar[XB_TOPGEN]) == tg, bar);
;             __builtin_amdgcn_fence(__ATOMIC_ACQUIRE, "agent");
.LBB0_121:
	s_andn2_saveexec_b64 s[0:1], s[0:1]
	s_cbranch_execz .LBB0_137
	v_mov_b32_e32 v1, s30
	v_add_co_u32_e32 v4, vcc, 0x3000, v1
	v_mov_b32_e32 v1, s31
	s_waitcnt vmcnt(0)
	v_addc_co_u32_e32 v5, vcc, 0, v1, vcc
	v_mov_b32_e32 v1, 1
	flat_atomic_add v1, v[4:5], v1 offset:1024 sc0
	v_cvt_f32_u32_e32 v3, v2
	v_sub_u32_e32 v4, 0, v2
	s_add_u32 s0, s30, 0x3400
	s_addc_u32 s1, s31, 0
	v_rcp_iflag_f32_e32 v3, v3
	s_mov_b64 s[4:5], 0
	v_mul_f32_e32 v3, 0x4f7ffffe, v3
	v_cvt_u32_f32_e32 v3, v3
	v_mul_lo_u32 v4, v4, v3
	v_mul_hi_u32 v4, v3, v4
	v_add_u32_e32 v3, v3, v4
	s_waitcnt vmcnt(0) lgkmcnt(0)
	v_mul_hi_u32 v3, v1, v3
	v_mul_lo_u32 v5, v3, v2
	v_add_u32_e32 v4, 1, v1
	v_sub_u32_e32 v1, v1, v5
	v_add_u32_e32 v6, 1, v3
	v_cmp_ge_u32_e32 vcc, v1, v2
	v_sub_u32_e32 v5, v1, v2
	s_nop 0
	v_cndmask_b32_e32 v3, v3, v6, vcc
	v_cndmask_b32_e32 v1, v1, v5, vcc
	v_add_u32_e32 v5, 1, v3
	v_cmp_ge_u32_e32 vcc, v1, v2
	s_nop 1
	v_cndmask_b32_e32 v1, v3, v5, vcc
	v_mad_u64_u32 v[2:3], s[2:3], v2, v1, v[2:3]
	v_cmp_ne_u32_e32 vcc, v4, v2
	v_mov_b32_e32 v4, v2
	v_mov_b64_e32 v[2:3], s[0:1]
	s_and_saveexec_b64 s[2:3], vcc
	s_cbranch_execz .LBB0_134
	v_mov_b64_e32 v[2:3], s[0:1]
	flat_load_dword v2, v[2:3] sc1
	s_mov_b64 s[8:9], 0
	s_waitcnt vmcnt(0) lgkmcnt(0)
	v_cmp_gt_u32_e32 vcc, v4, v2
	s_and_saveexec_b64 s[6:7], vcc
	s_cbranch_execz .LBB0_133
	s_add_u32 s4, s30, 0x200
	s_addc_u32 s5, s31, 0
	s_mov_b32 s21, 1
	s_branch .LBB0_126

; __device__ __forceinline__ unsigned xb_ld(unsigned* p)              { return __hip_atomic_load(p, __ATOMIC_RELAXED, __HIP_MEMORY_SCOPE_AGENT); }
; #define XB_SPIN(cond, bar) do { unsigned _sp = 0; while (cond) { __builtin_amdgcn_s_sleep(1); \
;     if ((++_sp & 255u) == 0u) { if (xb_ld(&(bar)[XB_TMO])) break; if (_sp > XB_SPIN_CAP) { atomicAdd(&(bar)[XB_TMO], 1u); break; } } } } while (0)
; __device__ __forceinline__ void xcd_barrier(const XcdBarrier& b) {
;     ...
;             else XB_SPIN(xb_ld(&bar[XB_TOPGEN]) == tg, bar);
.LBB0_131:
	v_mov_b64_e32 v[2:3], s[0:1]
	flat_load_dword v2, v[2:3] sc1
	s_add_i32 s21, s21, 1
	s_or_b64 s[12:13], s[12:13], exec
	s_waitcnt vmcnt(0) lgkmcnt(0)
	v_cmp_le_u32_e32 vcc, v4, v2
	s_orn2_b64 s[16:17], vcc, exec
	s_branch .LBB0_125

; __device__ __forceinline__ unsigned xb_ld(unsigned* p)              { return __hip_atomic_load(p, __ATOMIC_RELAXED, __HIP_MEMORY_SCOPE_AGENT); }
; __device__ __forceinline__ unsigned xb_add(unsigned* p, unsigned v) { return __hip_atomic_fetch_add(p, v, __ATOMIC_RELAXED, __HIP_MEMORY_SCOPE_AGENT); }
; #define XB_SPIN(cond, bar) do { unsigned _sp = 0; while (cond) { __builtin_amdgcn_s_sleep(1); \
;     if ((++_sp & 255u) == 0u) { if (xb_ld(&(bar)[XB_TMO])) break; if (_sp > XB_SPIN_CAP) { atomicAdd(&(bar)[XB_TMO], 1u); break; } } } } while (0)
; __device__ __forceinline__ void xcd_barrier(const XcdBarrier& b) {
;     ...
;         const unsigned old = xb_add(&bar[XB_XSUB(b.x)], 1u);
;         const unsigned gen = old / nloc;
;         if (old + 1u == (gen + 1u) * nloc) {
;             __builtin_amdgcn_fence(__ATOMIC_RELEASE, "agent");
;             asm volatile("s_waitcnt vmcnt(0)" ::: "memory");
;             const unsigned og = xb_add(&bar[XB_TOP], 1u);
;             const unsigned tg = og / nx;
;             if (og + 1u == (tg + 1u) * nx) xb_add(&bar[XB_TOPGEN], 1u);
;             else XB_SPIN(xb_ld(&bar[XB_TOPGEN]) == tg, bar);
;             __builtin_amdgcn_fence(__ATOMIC_ACQUIRE, "agent");
;             xb_add(&bar[XB_XGEN(b.x)], 1u);
;             asm volatile("s_waitcnt vmcnt(0)" ::: "memory");
;         } else {
;             XB_SPIN(xb_ld(&bar[XB_XGEN(b.x)]) == gen, bar);
.LBB0_766:
	s_lshl_b32 s1, s1, 6
	s_add_i32 s68, s1, 0x500
	s_lshl_b64 s[2:3], s[68:69], 2
	s_add_u32 s2, s34, s2
	s_addc_u32 s3, s35, s3
	v_mov_b64_e32 v[6:7], s[2:3]
	flat_atomic_add v6, v[6:7], v1 sc0
	v_cvt_f32_u32_e32 v5, v4
	v_sub_u32_e32 v7, 0, v4
	v_rcp_iflag_f32_e32 v5, v5
	s_nop 0
	v_mul_f32_e32 v5, 0x4f7ffffe, v5
	v_cvt_u32_f32_e32 v5, v5
	v_mul_lo_u32 v7, v7, v5
	v_mul_hi_u32 v7, v5, v7
	v_add_u32_e32 v5, v5, v7
	s_waitcnt vmcnt(0) lgkmcnt(0)
	v_mul_hi_u32 v5, v6, v5
	v_mul_lo_u32 v7, v5, v4
	v_sub_u32_e32 v7, v6, v7
	v_cmp_ge_u32_e32 vcc, v7, v4
	v_add_u32_e32 v8, 1, v5
	s_nop 0
	v_cndmask_b32_e32 v5, v5, v8, vcc
	v_sub_u32_e32 v8, v7, v4
	v_cndmask_b32_e32 v7, v7, v8, vcc
	v_cmp_ge_u32_e32 vcc, v7, v4
	v_add_u32_e32 v7, 1, v5
	v_add_u32_e32 v8, 1, v6
	v_cndmask_b32_e32 v5, v5, v7, vcc
	v_mad_u64_u32 v[6:7], s[2:3], v4, v5, v[4:5]
	v_cmp_ne_u32_e32 vcc, v8, v6
	s_and_saveexec_b64 s[2:3], vcc
	s_xor_b64 s[2:3], exec, s[2:3]
	s_cbranch_execz .LBB0_779
	v_mad_u32_u24 v5, v5, v2, v2
	s_movk_i32 s68, 0xd00
	s_lshl_b64 s[4:5], s[68:69], 2
	s_add_u32 s6, s34, s4
	s_addc_u32 s7, s35, s5
	v_mov_b64_e32 v[6:7], s[6:7]
	flat_load_dword v2, v[6:7] sc1
	s_waitcnt vmcnt(0) lgkmcnt(0)
	v_cmp_gt_u32_e32 vcc, v5, v2
	s_and_saveexec_b64 s[4:5], vcc
	s_cbranch_execz .LBB0_778
	s_mov_b32 s22, 1
	s_mov_b64 s[8:9], 0
	s_branch .LBB0_770

; __device__ __forceinline__ unsigned xb_ld(unsigned* p)              { return __hip_atomic_load(p, __ATOMIC_RELAXED, __HIP_MEMORY_SCOPE_AGENT); }
; #define XB_SPIN(cond, bar) do { unsigned _sp = 0; while (cond) { __builtin_amdgcn_s_sleep(1); \
;     if ((++_sp & 255u) == 0u) { if (xb_ld(&(bar)[XB_TMO])) break; if (_sp > XB_SPIN_CAP) { atomicAdd(&(bar)[XB_TMO], 1u); break; } } } } while (0)
; __device__ __forceinline__ void xcd_barrier(const XcdBarrier& b) {
;     ...
;             XB_SPIN(xb_ld(&bar[XB_XGEN(b.x)]) == gen, bar);
.LBB0_774:
	s_andn2_b64 s[12:13], s[12:13], exec
	s_and_b64 s[18:19], s[18:19], exec
	s_or_b64 s[12:13], s[12:13], s[18:19]
	s_and_saveexec_b64 s[18:19], s[16:17]
	s_cbranch_execz .LBB0_769
	v_mov_b64_e32 v[6:7], s[6:7]
	flat_load_dword v2, v[6:7] sc1
	s_add_i32 s22, s22, 1
	s_or_b64 s[12:13], s[12:13], exec
	s_waitcnt vmcnt(0) lgkmcnt(0)
	v_cmp_le_u32_e32 vcc, v5, v2
	s_orn2_b64 s[14:15], vcc, exec
	s_branch .LBB0_769

; __device__ __forceinline__ unsigned xb_ld(unsigned* p)              { return __hip_atomic_load(p, __ATOMIC_RELAXED, __HIP_MEMORY_SCOPE_AGENT); }
; __device__ __forceinline__ unsigned xb_add(unsigned* p, unsigned v) { return __hip_atomic_fetch_add(p, v, __ATOMIC_RELAXED, __HIP_MEMORY_SCOPE_AGENT); }
; #define XB_SPIN(cond, bar) do { unsigned _sp = 0; while (cond) { __builtin_amdgcn_s_sleep(1); \
;     if ((++_sp & 255u) == 0u) { if (xb_ld(&(bar)[XB_TMO])) break; if (_sp > XB_SPIN_CAP) { atomicAdd(&(bar)[XB_TMO], 1u); break; } } } } while (0)
; __device__ __forceinline__ void xcd_barrier(const XcdBarrier& b) {
;     ...
;         if (old + 1u == (gen + 1u) * nloc) {
;             __builtin_amdgcn_fence(__ATOMIC_RELEASE, "agent");
;             asm volatile("s_waitcnt vmcnt(0)" ::: "memory");
;             const unsigned og = xb_add(&bar[XB_TOP], 1u);
;             const unsigned tg = og / nx;
;             if (og + 1u == (tg + 1u) * nx) xb_add(&bar[XB_TOPGEN], 1u);
;             else XB_SPIN(xb_ld(&bar[XB_TOPGEN]) == tg, bar);
;             __builtin_amdgcn_fence(__ATOMIC_ACQUIRE, "agent");
.LBB0_779:
	s_andn2_saveexec_b64 s[2:3], s[2:3]
	s_cbranch_execz .LBB0_795
	v_mov_b32_e32 v4, s34
	v_add_co_u32_e32 v4, vcc, 0x3000, v4
	v_mov_b32_e32 v5, s35
	s_waitcnt vmcnt(0)
	v_addc_co_u32_e32 v5, vcc, 0, v5, vcc
	flat_atomic_add v4, v[4:5], v1 offset:1024 sc0
	v_cvt_f32_u32_e32 v5, v2
	v_sub_u32_e32 v6, 0, v2
	s_mov_b64 s[6:7], 0
	v_rcp_iflag_f32_e32 v5, v5
	s_nop 0
	v_mul_f32_e32 v5, 0x4f7ffffe, v5
	v_cvt_u32_f32_e32 v5, v5
	v_mul_lo_u32 v6, v6, v5
	v_mul_hi_u32 v6, v5, v6
	v_add_u32_e32 v5, v5, v6
	s_waitcnt vmcnt(0) lgkmcnt(0)
	v_mul_hi_u32 v5, v4, v5
	v_mul_lo_u32 v6, v5, v2
	v_sub_u32_e32 v6, v4, v6
	v_cmp_ge_u32_e32 vcc, v6, v2
	v_add_u32_e32 v7, 1, v5
	s_nop 0
	v_cndmask_b32_e32 v5, v5, v7, vcc
	v_sub_u32_e32 v7, v6, v2
	v_cndmask_b32_e32 v6, v6, v7, vcc
	v_cmp_ge_u32_e32 vcc, v6, v2
	v_add_u32_e32 v6, 1, v5
	v_add_u32_e32 v7, 1, v4
	v_cndmask_b32_e32 v6, v5, v6, vcc
	v_mad_u64_u32 v[4:5], s[2:3], v2, v6, v[2:3]
	s_add_u32 s2, s34, 0x3400
	s_addc_u32 s3, s35, 0
	v_cmp_ne_u32_e32 vcc, v7, v4
	v_mov_b32_e32 v7, v4
	v_mov_b64_e32 v[4:5], s[2:3]
	s_and_saveexec_b64 s[4:5], vcc
	s_cbranch_execz .LBB0_792
	v_mov_b64_e32 v[4:5], s[2:3]
	flat_load_dword v2, v[4:5] sc1
	s_mov_b64 s[10:11], 0
	s_waitcnt vmcnt(0) lgkmcnt(0)
	v_cmp_gt_u32_e32 vcc, v7, v2
	s_and_saveexec_b64 s[8:9], vcc
	s_cbranch_execz .LBB0_791
	s_add_u32 s6, s34, 0x200
	s_addc_u32 s7, s35, 0
	s_mov_b32 s22, 1
	s_branch .LBB0_784

; __device__ __forceinline__ unsigned xb_ld(unsigned* p)              { return __hip_atomic_load(p, __ATOMIC_RELAXED, __HIP_MEMORY_SCOPE_AGENT); }
; #define XB_SPIN(cond, bar) do { unsigned _sp = 0; while (cond) { __builtin_amdgcn_s_sleep(1); \
;     if ((++_sp & 255u) == 0u) { if (xb_ld(&(bar)[XB_TMO])) break; if (_sp > XB_SPIN_CAP) { atomicAdd(&(bar)[XB_TMO], 1u); break; } } } } while (0)
; __device__ __forceinline__ void xcd_barrier(const XcdBarrier& b) {
;     ...
;             else XB_SPIN(xb_ld(&bar[XB_TOPGEN]) == tg, bar);
.LBB0_789:
	v_mov_b64_e32 v[4:5], s[2:3]
	flat_load_dword v2, v[4:5] sc1
	s_add_i32 s22, s22, 1
	s_or_b64 s[16:17], s[16:17], exec
	s_waitcnt vmcnt(0) lgkmcnt(0)
	v_cmp_le_u32_e32 vcc, v7, v2
	s_orn2_b64 s[14:15], vcc, exec
	s_branch .LBB0_783

; __device__ __forceinline__ unsigned xb_ld(unsigned* p)              { return __hip_atomic_load(p, __ATOMIC_RELAXED, __HIP_MEMORY_SCOPE_AGENT); }
; __device__ __forceinline__ unsigned xb_add(unsigned* p, unsigned v) { return __hip_atomic_fetch_add(p, v, __ATOMIC_RELAXED, __HIP_MEMORY_SCOPE_AGENT); }
; #define XB_SPIN(cond, bar) do { unsigned _sp = 0; while (cond) { __builtin_amdgcn_s_sleep(1); \
;     if ((++_sp & 255u) == 0u) { if (xb_ld(&(bar)[XB_TMO])) break; if (_sp > XB_SPIN_CAP) { atomicAdd(&(bar)[XB_TMO], 1u); break; } } } } while (0)
; __device__ __forceinline__ void xcd_barrier(const XcdBarrier& b) {
;     ...
;         const unsigned old = xb_add(&bar[XB_XSUB(b.x)], 1u);
;         const unsigned gen = old / nloc;
;         if (old + 1u == (gen + 1u) * nloc) {
;             __builtin_amdgcn_fence(__ATOMIC_RELEASE, "agent");
;             asm volatile("s_waitcnt vmcnt(0)" ::: "memory");
;             const unsigned og = xb_add(&bar[XB_TOP], 1u);
;             const unsigned tg = og / nx;
;             if (og + 1u == (tg + 1u) * nx) xb_add(&bar[XB_TOPGEN], 1u);
;             else XB_SPIN(xb_ld(&bar[XB_TOPGEN]) == tg, bar);
;             __builtin_amdgcn_fence(__ATOMIC_ACQUIRE, "agent");
;             xb_add(&bar[XB_XGEN(b.x)], 1u);
;             asm volatile("s_waitcnt vmcnt(0)" ::: "memory");
;         } else {
;             XB_SPIN(xb_ld(&bar[XB_XGEN(b.x)]) == gen, bar);
.LBB0_845:
	s_lshl_b32 s1, s1, 6
	s_add_i32 s68, s1, 0x500
	s_lshl_b64 s[4:5], s[68:69], 2
	s_add_u32 s4, s40, s4
	s_addc_u32 s5, s41, s5
	v_mov_b64_e32 v[6:7], s[4:5]
	flat_atomic_add v6, v[6:7], v1 sc0
	v_cvt_f32_u32_e32 v5, v4
	v_sub_u32_e32 v7, 0, v4
	v_rcp_iflag_f32_e32 v5, v5
	s_nop 0
	v_mul_f32_e32 v5, 0x4f7ffffe, v5
	v_cvt_u32_f32_e32 v5, v5
	v_mul_lo_u32 v7, v7, v5
	v_mul_hi_u32 v7, v5, v7
	v_add_u32_e32 v5, v5, v7
	s_waitcnt vmcnt(0) lgkmcnt(0)
	v_mul_hi_u32 v5, v6, v5
	v_mul_lo_u32 v7, v5, v4
	v_sub_u32_e32 v7, v6, v7
	v_cmp_ge_u32_e32 vcc, v7, v4
	v_add_u32_e32 v8, 1, v5
	s_nop 0
	v_cndmask_b32_e32 v5, v5, v8, vcc
	v_sub_u32_e32 v8, v7, v4
	v_cndmask_b32_e32 v7, v7, v8, vcc
	v_cmp_ge_u32_e32 vcc, v7, v4
	v_add_u32_e32 v7, 1, v5
	v_add_u32_e32 v8, 1, v6
	v_cndmask_b32_e32 v5, v5, v7, vcc
	v_mad_u64_u32 v[6:7], s[4:5], v4, v5, v[4:5]
	v_cmp_ne_u32_e32 vcc, v8, v6
	s_and_saveexec_b64 s[4:5], vcc
	s_xor_b64 s[4:5], exec, s[4:5]
	s_cbranch_execz .LBB0_858
	v_mad_u32_u24 v5, v5, v2, v2
	s_movk_i32 s68, 0xd00
	s_lshl_b64 s[6:7], s[68:69], 2
	s_add_u32 s8, s40, s6
	s_addc_u32 s9, s41, s7
	v_mov_b64_e32 v[6:7], s[8:9]
	flat_load_dword v2, v[6:7] sc1
	s_waitcnt vmcnt(0) lgkmcnt(0)
	v_cmp_gt_u32_e32 vcc, v5, v2
	s_and_saveexec_b64 s[6:7], vcc
	s_cbranch_execz .LBB0_857
	s_mov_b32 s24, 1
	s_mov_b64 s[10:11], 0
	s_branch .LBB0_849

; __device__ __forceinline__ unsigned xb_ld(unsigned* p)              { return __hip_atomic_load(p, __ATOMIC_RELAXED, __HIP_MEMORY_SCOPE_AGENT); }
; #define XB_SPIN(cond, bar) do { unsigned _sp = 0; while (cond) { __builtin_amdgcn_s_sleep(1); \
;     if ((++_sp & 255u) == 0u) { if (xb_ld(&(bar)[XB_TMO])) break; if (_sp > XB_SPIN_CAP) { atomicAdd(&(bar)[XB_TMO], 1u); break; } } } } while (0)
; __device__ __forceinline__ void xcd_barrier(const XcdBarrier& b) {
;     ...
;             XB_SPIN(xb_ld(&bar[XB_XGEN(b.x)]) == gen, bar);
.LBB0_853:
	s_andn2_b64 s[14:15], s[14:15], exec
	s_and_b64 s[20:21], s[20:21], exec
	s_or_b64 s[14:15], s[14:15], s[20:21]
	s_and_saveexec_b64 s[20:21], s[18:19]
	s_cbranch_execz .LBB0_848
	v_mov_b64_e32 v[6:7], s[8:9]
	flat_load_dword v2, v[6:7] sc1
	s_add_i32 s24, s24, 1
	s_or_b64 s[14:15], s[14:15], exec
	s_waitcnt vmcnt(0) lgkmcnt(0)
	v_cmp_le_u32_e32 vcc, v5, v2
	s_orn2_b64 s[16:17], vcc, exec
	s_branch .LBB0_848

; __device__ __forceinline__ unsigned xb_ld(unsigned* p)              { return __hip_atomic_load(p, __ATOMIC_RELAXED, __HIP_MEMORY_SCOPE_AGENT); }
; __device__ __forceinline__ unsigned xb_add(unsigned* p, unsigned v) { return __hip_atomic_fetch_add(p, v, __ATOMIC_RELAXED, __HIP_MEMORY_SCOPE_AGENT); }
; #define XB_SPIN(cond, bar) do { unsigned _sp = 0; while (cond) { __builtin_amdgcn_s_sleep(1); \
;     if ((++_sp & 255u) == 0u) { if (xb_ld(&(bar)[XB_TMO])) break; if (_sp > XB_SPIN_CAP) { atomicAdd(&(bar)[XB_TMO], 1u); break; } } } } while (0)
; __device__ __forceinline__ void xcd_barrier(const XcdBarrier& b) {
;     ...
;         if (old + 1u == (gen + 1u) * nloc) {
;             __builtin_amdgcn_fence(__ATOMIC_RELEASE, "agent");
;             asm volatile("s_waitcnt vmcnt(0)" ::: "memory");
;             const unsigned og = xb_add(&bar[XB_TOP], 1u);
;             const unsigned tg = og / nx;
;             if (og + 1u == (tg + 1u) * nx) xb_add(&bar[XB_TOPGEN], 1u);
;             else XB_SPIN(xb_ld(&bar[XB_TOPGEN]) == tg, bar);
;             __builtin_amdgcn_fence(__ATOMIC_ACQUIRE, "agent");
.LBB0_858:
	s_andn2_saveexec_b64 s[4:5], s[4:5]
	s_cbranch_execz .LBB0_874
	v_mov_b32_e32 v4, s40
	v_add_co_u32_e32 v4, vcc, 0x3000, v4
	v_mov_b32_e32 v5, s41
	s_waitcnt vmcnt(0)
	v_addc_co_u32_e32 v5, vcc, 0, v5, vcc
	flat_atomic_add v4, v[4:5], v1 offset:1024 sc0
	v_cvt_f32_u32_e32 v5, v2
	v_sub_u32_e32 v6, 0, v2
	s_mov_b64 s[8:9], 0
	v_rcp_iflag_f32_e32 v5, v5
	s_nop 0
	v_mul_f32_e32 v5, 0x4f7ffffe, v5
	v_cvt_u32_f32_e32 v5, v5
	v_mul_lo_u32 v6, v6, v5
	v_mul_hi_u32 v6, v5, v6
	v_add_u32_e32 v5, v5, v6
	s_waitcnt vmcnt(0) lgkmcnt(0)
	v_mul_hi_u32 v5, v4, v5
	v_mul_lo_u32 v6, v5, v2
	v_sub_u32_e32 v6, v4, v6
	v_cmp_ge_u32_e32 vcc, v6, v2
	v_add_u32_e32 v7, 1, v5
	s_nop 0
	v_cndmask_b32_e32 v5, v5, v7, vcc
	v_sub_u32_e32 v7, v6, v2
	v_cndmask_b32_e32 v6, v6, v7, vcc
	v_cmp_ge_u32_e32 vcc, v6, v2
	v_add_u32_e32 v6, 1, v5
	v_add_u32_e32 v7, 1, v4
	v_cndmask_b32_e32 v6, v5, v6, vcc
	v_mad_u64_u32 v[4:5], s[4:5], v2, v6, v[2:3]
	s_add_u32 s4, s40, 0x3400
	s_addc_u32 s5, s41, 0
	v_cmp_ne_u32_e32 vcc, v7, v4
	v_mov_b32_e32 v7, v4
	v_mov_b64_e32 v[4:5], s[4:5]
	s_and_saveexec_b64 s[6:7], vcc
	s_cbranch_execz .LBB0_871
	v_mov_b64_e32 v[4:5], s[4:5]
	flat_load_dword v2, v[4:5] sc1
	s_mov_b64 s[12:13], 0
	s_waitcnt vmcnt(0) lgkmcnt(0)
	v_cmp_gt_u32_e32 vcc, v7, v2
	s_and_saveexec_b64 s[10:11], vcc
	s_cbranch_execz .LBB0_870
	s_add_u32 s8, s40, 0x200
	s_addc_u32 s9, s41, 0
	s_mov_b32 s24, 1
	s_branch .LBB0_863

; __device__ __forceinline__ unsigned xb_ld(unsigned* p)              { return __hip_atomic_load(p, __ATOMIC_RELAXED, __HIP_MEMORY_SCOPE_AGENT); }
; #define XB_SPIN(cond, bar) do { unsigned _sp = 0; while (cond) { __builtin_amdgcn_s_sleep(1); \
;     if ((++_sp & 255u) == 0u) { if (xb_ld(&(bar)[XB_TMO])) break; if (_sp > XB_SPIN_CAP) { atomicAdd(&(bar)[XB_TMO], 1u); break; } } } } while (0)
; __device__ __forceinline__ void xcd_barrier(const XcdBarrier& b) {
;     ...
;             else XB_SPIN(xb_ld(&bar[XB_TOPGEN]) == tg, bar);
.LBB0_868:
	v_mov_b64_e32 v[4:5], s[4:5]
	flat_load_dword v2, v[4:5] sc1
	s_add_i32 s24, s24, 1
	s_or_b64 s[18:19], s[18:19], exec
	s_waitcnt vmcnt(0) lgkmcnt(0)
	v_cmp_le_u32_e32 vcc, v7, v2
	s_orn2_b64 s[16:17], vcc, exec
	s_branch .LBB0_862

; __device__ __forceinline__ unsigned xb_ld(unsigned* p)              { return __hip_atomic_load(p, __ATOMIC_RELAXED, __HIP_MEMORY_SCOPE_AGENT); }
; __device__ __forceinline__ unsigned xb_add(unsigned* p, unsigned v) { return __hip_atomic_fetch_add(p, v, __ATOMIC_RELAXED, __HIP_MEMORY_SCOPE_AGENT); }
; #define XB_SPIN(cond, bar) do { unsigned _sp = 0; while (cond) { __builtin_amdgcn_s_sleep(1); \
;     if ((++_sp & 255u) == 0u) { if (xb_ld(&(bar)[XB_TMO])) break; if (_sp > XB_SPIN_CAP) { atomicAdd(&(bar)[XB_TMO], 1u); break; } } } } while (0)
; __device__ __forceinline__ void xcd_barrier(const XcdBarrier& b) {
;     ...
;         const unsigned old = xb_add(&bar[XB_XSUB(b.x)], 1u);
;         const unsigned gen = old / nloc;
;         if (old + 1u == (gen + 1u) * nloc) {
;             __builtin_amdgcn_fence(__ATOMIC_RELEASE, "agent");
;             asm volatile("s_waitcnt vmcnt(0)" ::: "memory");
;             const unsigned og = xb_add(&bar[XB_TOP], 1u);
;             const unsigned tg = og / nx;
;             if (og + 1u == (tg + 1u) * nx) xb_add(&bar[XB_TOPGEN], 1u);
;             else XB_SPIN(xb_ld(&bar[XB_TOPGEN]) == tg, bar);
;             __builtin_amdgcn_fence(__ATOMIC_ACQUIRE, "agent");
;             xb_add(&bar[XB_XGEN(b.x)], 1u);
;             asm volatile("s_waitcnt vmcnt(0)" ::: "memory");
;         } else {
;             XB_SPIN(xb_ld(&bar[XB_XGEN(b.x)]) == gen, bar);
.LBB0_1774:
	s_lshl_b32 s0, s0, 6
	s_add_i32 s68, s0, 0x500
	s_lshl_b64 s[2:3], s[68:69], 2
	s_add_u32 s2, s34, s2
	s_addc_u32 s3, s35, s3
	v_mov_b64_e32 v[6:7], s[2:3]
	flat_atomic_add v6, v[6:7], v1 sc0
	v_cvt_f32_u32_e32 v5, v4
	v_sub_u32_e32 v7, 0, v4
	v_rcp_iflag_f32_e32 v5, v5
	s_nop 0
	v_mul_f32_e32 v5, 0x4f7ffffe, v5
	v_cvt_u32_f32_e32 v5, v5
	v_mul_lo_u32 v7, v7, v5
	v_mul_hi_u32 v7, v5, v7
	v_add_u32_e32 v5, v5, v7
	s_waitcnt vmcnt(0) lgkmcnt(0)
	v_mul_hi_u32 v5, v6, v5
	v_mul_lo_u32 v7, v5, v4
	v_sub_u32_e32 v7, v6, v7
	v_cmp_ge_u32_e32 vcc, v7, v4
	v_add_u32_e32 v8, 1, v5
	s_nop 0
	v_cndmask_b32_e32 v5, v5, v8, vcc
	v_sub_u32_e32 v8, v7, v4
	v_cndmask_b32_e32 v7, v7, v8, vcc
	v_cmp_ge_u32_e32 vcc, v7, v4
	v_add_u32_e32 v7, 1, v5
	v_add_u32_e32 v8, 1, v6
	v_cndmask_b32_e32 v5, v5, v7, vcc
	v_mad_u64_u32 v[6:7], s[2:3], v4, v5, v[4:5]
	v_cmp_ne_u32_e32 vcc, v8, v6
	s_and_saveexec_b64 s[2:3], vcc
	s_xor_b64 s[2:3], exec, s[2:3]
	s_cbranch_execz .LBB0_1787
	v_mad_u32_u24 v5, v5, v2, v2
	s_movk_i32 s68, 0xd00
	s_lshl_b64 s[4:5], s[68:69], 2
	s_add_u32 s6, s34, s4
	s_addc_u32 s7, s35, s5
	v_mov_b64_e32 v[6:7], s[6:7]
	flat_load_dword v2, v[6:7] sc1
	s_waitcnt vmcnt(0) lgkmcnt(0)
	v_cmp_gt_u32_e32 vcc, v5, v2
	s_and_saveexec_b64 s[4:5], vcc
	s_cbranch_execz .LBB0_1786
	s_mov_b32 s1, 1
	s_mov_b64 s[8:9], 0
	s_branch .LBB0_1778

; __device__ __forceinline__ unsigned xb_ld(unsigned* p)              { return __hip_atomic_load(p, __ATOMIC_RELAXED, __HIP_MEMORY_SCOPE_AGENT); }
; __device__ __forceinline__ unsigned xb_add(unsigned* p, unsigned v) { return __hip_atomic_fetch_add(p, v, __ATOMIC_RELAXED, __HIP_MEMORY_SCOPE_AGENT); }
; #define XB_SPIN(cond, bar) do { unsigned _sp = 0; while (cond) { __builtin_amdgcn_s_sleep(1); \
;     if ((++_sp & 255u) == 0u) { if (xb_ld(&(bar)[XB_TMO])) break; if (_sp > XB_SPIN_CAP) { atomicAdd(&(bar)[XB_TMO], 1u); break; } } } } while (0)
; __device__ __forceinline__ void xcd_barrier(const XcdBarrier& b) {
;     ...
;             const unsigned og = xb_add(&bar[XB_TOP], 1u);
;             const unsigned tg = og / nx;
;             if (og + 1u == (tg + 1u) * nx) xb_add(&bar[XB_TOPGEN], 1u);
;             else XB_SPIN(xb_ld(&bar[XB_TOPGEN]) == tg, bar);
.LBB0_1782:
	s_andn2_b64 s[12:13], s[12:13], exec
	s_and_b64 s[18:19], s[18:19], exec
	s_or_b64 s[12:13], s[12:13], s[18:19]
	s_and_saveexec_b64 s[18:19], s[16:17]
	s_cbranch_execz .LBB0_1777
	v_mov_b64_e32 v[6:7], s[6:7]
	flat_load_dword v2, v[6:7] sc1
	s_add_i32 s1, s1, 1
	s_or_b64 s[12:13], s[12:13], exec
	s_waitcnt vmcnt(0) lgkmcnt(0)
	v_cmp_le_u32_e32 vcc, v5, v2
	s_orn2_b64 s[14:15], vcc, exec
	s_branch .LBB0_1777

; __device__ __forceinline__ unsigned xb_ld(unsigned* p)              { return __hip_atomic_load(p, __ATOMIC_RELAXED, __HIP_MEMORY_SCOPE_AGENT); }
; __device__ __forceinline__ unsigned xb_add(unsigned* p, unsigned v) { return __hip_atomic_fetch_add(p, v, __ATOMIC_RELAXED, __HIP_MEMORY_SCOPE_AGENT); }
; #define XB_SPIN(cond, bar) do { unsigned _sp = 0; while (cond) { __builtin_amdgcn_s_sleep(1); \
;     if ((++_sp & 255u) == 0u) { if (xb_ld(&(bar)[XB_TMO])) break; if (_sp > XB_SPIN_CAP) { atomicAdd(&(bar)[XB_TMO], 1u); break; } } } } while (0)
; __device__ __forceinline__ void xcd_barrier(const XcdBarrier& b) {
;     ...
;             const unsigned og = xb_add(&bar[XB_TOP], 1u);
;             const unsigned tg = og / nx;
;             if (og + 1u == (tg + 1u) * nx) xb_add(&bar[XB_TOPGEN], 1u);
;             else XB_SPIN(xb_ld(&bar[XB_TOPGEN]) == tg, bar);
.LBB0_1787:
	s_andn2_saveexec_b64 s[2:3], s[2:3]
	s_cbranch_execz .LBB0_1803
	v_mov_b32_e32 v4, s34
	v_add_co_u32_e32 v4, vcc, 0x3000, v4
	v_mov_b32_e32 v5, s35
	s_waitcnt vmcnt(0)
	v_addc_co_u32_e32 v5, vcc, 0, v5, vcc
	flat_atomic_add v4, v[4:5], v1 offset:1024 sc0
	v_cvt_f32_u32_e32 v5, v2
	v_sub_u32_e32 v6, 0, v2
	s_mov_b64 s[6:7], 0
	v_rcp_iflag_f32_e32 v5, v5
	s_nop 0
	v_mul_f32_e32 v5, 0x4f7ffffe, v5
	v_cvt_u32_f32_e32 v5, v5
	v_mul_lo_u32 v6, v6, v5
	v_mul_hi_u32 v6, v5, v6
	v_add_u32_e32 v5, v5, v6
	s_waitcnt vmcnt(0) lgkmcnt(0)
	v_mul_hi_u32 v5, v4, v5
	v_mul_lo_u32 v6, v5, v2
	v_sub_u32_e32 v6, v4, v6
	v_cmp_ge_u32_e32 vcc, v6, v2
	v_add_u32_e32 v7, 1, v5
	s_nop 0
	v_cndmask_b32_e32 v5, v5, v7, vcc
	v_sub_u32_e32 v7, v6, v2
	v_cndmask_b32_e32 v6, v6, v7, vcc
	v_cmp_ge_u32_e32 vcc, v6, v2
	v_add_u32_e32 v6, 1, v5
	v_add_u32_e32 v7, 1, v4
	v_cndmask_b32_e32 v6, v5, v6, vcc
	v_mad_u64_u32 v[4:5], s[2:3], v2, v6, v[2:3]
	s_add_u32 s2, s34, 0x3400
	s_addc_u32 s3, s35, 0
	v_cmp_ne_u32_e32 vcc, v7, v4
	v_mov_b32_e32 v7, v4
	v_mov_b64_e32 v[4:5], s[2:3]
	s_and_saveexec_b64 s[4:5], vcc
	s_cbranch_execz .LBB0_1800
	v_mov_b64_e32 v[4:5], s[2:3]
	flat_load_dword v2, v[4:5] sc1
	s_mov_b64 s[10:11], 0
	s_waitcnt vmcnt(0) lgkmcnt(0)
	v_cmp_gt_u32_e32 vcc, v7, v2
	s_and_saveexec_b64 s[8:9], vcc
	s_cbranch_execz .LBB0_1799
	s_add_u32 s6, s34, 0x200
	s_addc_u32 s7, s35, 0
	s_mov_b32 s1, 1
	s_branch .LBB0_1792

; __device__ __forceinline__ unsigned xb_ld(unsigned* p)              { return __hip_atomic_load(p, __ATOMIC_RELAXED, __HIP_MEMORY_SCOPE_AGENT); }
; __device__ __forceinline__ unsigned xb_add(unsigned* p, unsigned v) { return __hip_atomic_fetch_add(p, v, __ATOMIC_RELAXED, __HIP_MEMORY_SCOPE_AGENT); }
; #define XB_SPIN(cond, bar) do { unsigned _sp = 0; while (cond) { __builtin_amdgcn_s_sleep(1); \
;     if ((++_sp & 255u) == 0u) { if (xb_ld(&(bar)[XB_TMO])) break; if (_sp > XB_SPIN_CAP) { atomicAdd(&(bar)[XB_TMO], 1u); break; } } } } while (0)
; __device__ __forceinline__ void xcd_barrier(const XcdBarrier& b) {
;     ...
;             const unsigned og = xb_add(&bar[XB_TOP], 1u);
;             const unsigned tg = og / nx;
;             if (og + 1u == (tg + 1u) * nx) xb_add(&bar[XB_TOPGEN], 1u);
;             else XB_SPIN(xb_ld(&bar[XB_TOPGEN]) == tg, bar);
.LBB0_1797:
	v_mov_b64_e32 v[4:5], s[2:3]
	flat_load_dword v2, v[4:5] sc1
	s_add_i32 s1, s1, 1
	s_or_b64 s[16:17], s[16:17], exec
	s_waitcnt vmcnt(0) lgkmcnt(0)
	v_cmp_le_u32_e32 vcc, v7, v2
	s_orn2_b64 s[14:15], vcc, exec
	s_branch .LBB0_1791
